# moe_tables at the head of both MoE phases: 24 serial ds_read_b32+lgkmcnt(0) steps replaced by six ds_read_b128 up front and 24 register steps; on top of v62
# speedup vs baseline: 1.0024x; 1.0024x over previous
.LBB0_1001:
	s_or_b64 exec, exec, s[6:7]
	s_movk_i32 s0, 0x80
	v_cmp_gt_u32_e32 vcc, s0, v0
	s_waitcnt lgkmcnt(0)
	s_barrier
	s_and_saveexec_b64 s[6:7], vcc
	s_cbranch_execz .LBB0_1006
	s_mov_b32 s0, 0
	s_add_i32 s1, 0, 0x22400
	v_mov_b32_e32 v1, -1
	v_mov_b32_e32 v3, 0
	v_mov_b32_e32 v2, 0
	v_mov_b32_e32 v4, s1
	ds_read_b128 v[100:103], v4
	ds_read_b128 v[104:107], v4 offset:16
	ds_read_b128 v[108:111], v4 offset:32
	ds_read_b128 v[112:115], v4 offset:48
	ds_read_b128 v[116:119], v4 offset:64
	ds_read_b128 v[120:123], v4 offset:80
	s_waitcnt lgkmcnt(0)
	v_sub_u32_e32 v6, v0, v3
	v_cmp_gt_i32_e32 vcc, 0, v1
	v_mov_b32_e32 v5, 0
	v_add_u32_e32 v3, v100, v3
	v_cmp_lt_i32_e64 s[4:5], v0, v3
	s_nop 0
	s_and_b64 vcc, vcc, s[4:5]
	v_cndmask_b32_e32 v2, v2, v6, vcc
	v_cndmask_b32_e32 v1, v1, v5, vcc
	v_sub_u32_e32 v6, v0, v3
	v_cmp_gt_i32_e32 vcc, 0, v1
	v_mov_b32_e32 v5, 1
	v_add_u32_e32 v3, v101, v3
	v_cmp_lt_i32_e64 s[4:5], v0, v3
	s_nop 0
	s_and_b64 vcc, vcc, s[4:5]
	v_cndmask_b32_e32 v2, v2, v6, vcc
	v_cndmask_b32_e32 v1, v1, v5, vcc
	v_sub_u32_e32 v6, v0, v3
	v_cmp_gt_i32_e32 vcc, 0, v1
	v_mov_b32_e32 v5, 2
	v_add_u32_e32 v3, v102, v3
	v_cmp_lt_i32_e64 s[4:5], v0, v3
	s_nop 0
	s_and_b64 vcc, vcc, s[4:5]
	v_cndmask_b32_e32 v2, v2, v6, vcc
	v_cndmask_b32_e32 v1, v1, v5, vcc
	v_sub_u32_e32 v6, v0, v3
	v_cmp_gt_i32_e32 vcc, 0, v1
	v_mov_b32_e32 v5, 3
	v_add_u32_e32 v3, v103, v3
	v_cmp_lt_i32_e64 s[4:5], v0, v3
	s_nop 0
	s_and_b64 vcc, vcc, s[4:5]
	v_cndmask_b32_e32 v2, v2, v6, vcc
	v_cndmask_b32_e32 v1, v1, v5, vcc
	v_sub_u32_e32 v6, v0, v3
	v_cmp_gt_i32_e32 vcc, 0, v1
	v_mov_b32_e32 v5, 4
	v_add_u32_e32 v3, v104, v3
	v_cmp_lt_i32_e64 s[4:5], v0, v3
	s_nop 0
	s_and_b64 vcc, vcc, s[4:5]
	v_cndmask_b32_e32 v2, v2, v6, vcc
	v_cndmask_b32_e32 v1, v1, v5, vcc
	v_sub_u32_e32 v6, v0, v3
	v_cmp_gt_i32_e32 vcc, 0, v1
	v_mov_b32_e32 v5, 5
	v_add_u32_e32 v3, v105, v3
	v_cmp_lt_i32_e64 s[4:5], v0, v3
	s_nop 0
	s_and_b64 vcc, vcc, s[4:5]
	v_cndmask_b32_e32 v2, v2, v6, vcc
	v_cndmask_b32_e32 v1, v1, v5, vcc
	v_sub_u32_e32 v6, v0, v3
	v_cmp_gt_i32_e32 vcc, 0, v1
	v_mov_b32_e32 v5, 6
	v_add_u32_e32 v3, v106, v3
	v_cmp_lt_i32_e64 s[4:5], v0, v3
	s_nop 0
	s_and_b64 vcc, vcc, s[4:5]
	v_cndmask_b32_e32 v2, v2, v6, vcc
	v_cndmask_b32_e32 v1, v1, v5, vcc
	v_sub_u32_e32 v6, v0, v3
	v_cmp_gt_i32_e32 vcc, 0, v1
	v_mov_b32_e32 v5, 7
	v_add_u32_e32 v3, v107, v3
	v_cmp_lt_i32_e64 s[4:5], v0, v3
	s_nop 0
	s_and_b64 vcc, vcc, s[4:5]
	v_cndmask_b32_e32 v2, v2, v6, vcc
	v_cndmask_b32_e32 v1, v1, v5, vcc
	v_sub_u32_e32 v6, v0, v3
	v_cmp_gt_i32_e32 vcc, 0, v1
	v_mov_b32_e32 v5, 8
	v_add_u32_e32 v3, v108, v3
	v_cmp_lt_i32_e64 s[4:5], v0, v3
	s_nop 0
	s_and_b64 vcc, vcc, s[4:5]
	v_cndmask_b32_e32 v2, v2, v6, vcc
	v_cndmask_b32_e32 v1, v1, v5, vcc
	v_sub_u32_e32 v6, v0, v3
	v_cmp_gt_i32_e32 vcc, 0, v1
	v_mov_b32_e32 v5, 9
	v_add_u32_e32 v3, v109, v3
	v_cmp_lt_i32_e64 s[4:5], v0, v3
	s_nop 0
	s_and_b64 vcc, vcc, s[4:5]
	v_cndmask_b32_e32 v2, v2, v6, vcc
	v_cndmask_b32_e32 v1, v1, v5, vcc
	v_sub_u32_e32 v6, v0, v3
	v_cmp_gt_i32_e32 vcc, 0, v1
	v_mov_b32_e32 v5, 10
	v_add_u32_e32 v3, v110, v3
	v_cmp_lt_i32_e64 s[4:5], v0, v3
	s_nop 0
	s_and_b64 vcc, vcc, s[4:5]
	v_cndmask_b32_e32 v2, v2, v6, vcc
	v_cndmask_b32_e32 v1, v1, v5, vcc
	v_sub_u32_e32 v6, v0, v3
	v_cmp_gt_i32_e32 vcc, 0, v1
	v_mov_b32_e32 v5, 11
	v_add_u32_e32 v3, v111, v3
	v_cmp_lt_i32_e64 s[4:5], v0, v3
	s_nop 0
	s_and_b64 vcc, vcc, s[4:5]
	v_cndmask_b32_e32 v2, v2, v6, vcc
	v_cndmask_b32_e32 v1, v1, v5, vcc
	v_sub_u32_e32 v6, v0, v3
	v_cmp_gt_i32_e32 vcc, 0, v1
	v_mov_b32_e32 v5, 12
	v_add_u32_e32 v3, v112, v3
	v_cmp_lt_i32_e64 s[4:5], v0, v3
	s_nop 0
	s_and_b64 vcc, vcc, s[4:5]
	v_cndmask_b32_e32 v2, v2, v6, vcc
	v_cndmask_b32_e32 v1, v1, v5, vcc
	v_sub_u32_e32 v6, v0, v3
	v_cmp_gt_i32_e32 vcc, 0, v1
	v_mov_b32_e32 v5, 13
	v_add_u32_e32 v3, v113, v3
	v_cmp_lt_i32_e64 s[4:5], v0, v3
	s_nop 0
	s_and_b64 vcc, vcc, s[4:5]
	v_cndmask_b32_e32 v2, v2, v6, vcc
	v_cndmask_b32_e32 v1, v1, v5, vcc
	v_sub_u32_e32 v6, v0, v3
	v_cmp_gt_i32_e32 vcc, 0, v1
	v_mov_b32_e32 v5, 14
	v_add_u32_e32 v3, v114, v3
	v_cmp_lt_i32_e64 s[4:5], v0, v3
	s_nop 0
	s_and_b64 vcc, vcc, s[4:5]
	v_cndmask_b32_e32 v2, v2, v6, vcc
	v_cndmask_b32_e32 v1, v1, v5, vcc
	v_sub_u32_e32 v6, v0, v3
	v_cmp_gt_i32_e32 vcc, 0, v1
	v_mov_b32_e32 v5, 15
	v_add_u32_e32 v3, v115, v3
	v_cmp_lt_i32_e64 s[4:5], v0, v3
	s_nop 0
	s_and_b64 vcc, vcc, s[4:5]
	v_cndmask_b32_e32 v2, v2, v6, vcc
	v_cndmask_b32_e32 v1, v1, v5, vcc
	v_sub_u32_e32 v6, v0, v3
	v_cmp_gt_i32_e32 vcc, 0, v1
	v_mov_b32_e32 v5, 16
	v_add_u32_e32 v3, v116, v3
	v_cmp_lt_i32_e64 s[4:5], v0, v3
	s_nop 0
	s_and_b64 vcc, vcc, s[4:5]
	v_cndmask_b32_e32 v2, v2, v6, vcc
	v_cndmask_b32_e32 v1, v1, v5, vcc
	v_sub_u32_e32 v6, v0, v3
	v_cmp_gt_i32_e32 vcc, 0, v1
	v_mov_b32_e32 v5, 17
	v_add_u32_e32 v3, v117, v3
	v_cmp_lt_i32_e64 s[4:5], v0, v3
	s_nop 0
	s_and_b64 vcc, vcc, s[4:5]
	v_cndmask_b32_e32 v2, v2, v6, vcc
	v_cndmask_b32_e32 v1, v1, v5, vcc
	v_sub_u32_e32 v6, v0, v3
	v_cmp_gt_i32_e32 vcc, 0, v1
	v_mov_b32_e32 v5, 18
	v_add_u32_e32 v3, v118, v3
	v_cmp_lt_i32_e64 s[4:5], v0, v3
	s_nop 0
	s_and_b64 vcc, vcc, s[4:5]
	v_cndmask_b32_e32 v2, v2, v6, vcc
	v_cndmask_b32_e32 v1, v1, v5, vcc
	v_sub_u32_e32 v6, v0, v3
	v_cmp_gt_i32_e32 vcc, 0, v1
	v_mov_b32_e32 v5, 19
	v_add_u32_e32 v3, v119, v3
	v_cmp_lt_i32_e64 s[4:5], v0, v3
	s_nop 0
	s_and_b64 vcc, vcc, s[4:5]
	v_cndmask_b32_e32 v2, v2, v6, vcc
	v_cndmask_b32_e32 v1, v1, v5, vcc
	v_sub_u32_e32 v6, v0, v3
	v_cmp_gt_i32_e32 vcc, 0, v1
	v_mov_b32_e32 v5, 20
	v_add_u32_e32 v3, v120, v3
	v_cmp_lt_i32_e64 s[4:5], v0, v3
	s_nop 0
	s_and_b64 vcc, vcc, s[4:5]
	v_cndmask_b32_e32 v2, v2, v6, vcc
	v_cndmask_b32_e32 v1, v1, v5, vcc
	v_sub_u32_e32 v6, v0, v3
	v_cmp_gt_i32_e32 vcc, 0, v1
	v_mov_b32_e32 v5, 21
	v_add_u32_e32 v3, v121, v3
	v_cmp_lt_i32_e64 s[4:5], v0, v3
	s_nop 0
	s_and_b64 vcc, vcc, s[4:5]
	v_cndmask_b32_e32 v2, v2, v6, vcc
	v_cndmask_b32_e32 v1, v1, v5, vcc
	v_sub_u32_e32 v6, v0, v3
	v_cmp_gt_i32_e32 vcc, 0, v1
	v_mov_b32_e32 v5, 22
	v_add_u32_e32 v3, v122, v3
	v_cmp_lt_i32_e64 s[4:5], v0, v3
	s_nop 0
	s_and_b64 vcc, vcc, s[4:5]
	v_cndmask_b32_e32 v2, v2, v6, vcc
	v_cndmask_b32_e32 v1, v1, v5, vcc
	v_sub_u32_e32 v6, v0, v3
	v_cmp_gt_i32_e32 vcc, 0, v1
	v_mov_b32_e32 v5, 23
	v_add_u32_e32 v3, v123, v3
	v_cmp_lt_i32_e64 s[4:5], v0, v3
	s_nop 0
	s_and_b64 vcc, vcc, s[4:5]
	v_cndmask_b32_e32 v2, v2, v6, vcc
	v_cndmask_b32_e32 v1, v1, v5, vcc
	v_lshl_or_b32 v2, v1, 16, v2
	v_cmp_lt_i32_e32 vcc, -1, v1
	s_add_i32 s0, 0, 0x22400
	s_nop 0
	v_cndmask_b32_e32 v1, -1, v2, vcc
	v_lshl_add_u32 v2, v0, 2, s0
	ds_write_b32 v2, v1 offset:256
	s_and_b64 exec, exec, s[78:79]
	s_add_i32 s0, 0, 0x224f0
	v_mov_b32_e32 v1, s0
	ds_write_b32 v1, v3

.LBB0_2048:
	s_or_b64 exec, exec, s[0:1]
	s_movk_i32 s0, 0x80
	v_cmp_gt_u32_e32 vcc, s0, v0
	s_waitcnt lgkmcnt(0)
	s_barrier
	s_and_saveexec_b64 s[0:1], vcc
	s_cbranch_execz .LBB0_2053
	s_mov_b32 s4, 0
	s_add_i32 s5, 0, 0x22400
	v_mov_b32_e32 v1, -1
	v_mov_b32_e32 v3, 0
	v_mov_b32_e32 v2, 0
	v_mov_b32_e32 v4, s5
	ds_read_b128 v[100:103], v4
	ds_read_b128 v[104:107], v4 offset:16
	ds_read_b128 v[108:111], v4 offset:32
	ds_read_b128 v[112:115], v4 offset:48
	ds_read_b128 v[116:119], v4 offset:64
	ds_read_b128 v[120:123], v4 offset:80
	s_waitcnt lgkmcnt(0)
	v_sub_u32_e32 v6, v0, v3
	v_cmp_gt_i32_e32 vcc, 0, v1
	v_mov_b32_e32 v5, 0
	v_add_u32_e32 v3, v100, v3
	v_cmp_lt_i32_e64 s[2:3], v0, v3
	s_nop 0
	s_and_b64 vcc, vcc, s[2:3]
	v_cndmask_b32_e32 v2, v2, v6, vcc
	v_cndmask_b32_e32 v1, v1, v5, vcc
	v_sub_u32_e32 v6, v0, v3
	v_cmp_gt_i32_e32 vcc, 0, v1
	v_mov_b32_e32 v5, 1
	v_add_u32_e32 v3, v101, v3
	v_cmp_lt_i32_e64 s[2:3], v0, v3
	s_nop 0
	s_and_b64 vcc, vcc, s[2:3]
	v_cndmask_b32_e32 v2, v2, v6, vcc
	v_cndmask_b32_e32 v1, v1, v5, vcc
	v_sub_u32_e32 v6, v0, v3
	v_cmp_gt_i32_e32 vcc, 0, v1
	v_mov_b32_e32 v5, 2
	v_add_u32_e32 v3, v102, v3
	v_cmp_lt_i32_e64 s[2:3], v0, v3
	s_nop 0
	s_and_b64 vcc, vcc, s[2:3]
	v_cndmask_b32_e32 v2, v2, v6, vcc
	v_cndmask_b32_e32 v1, v1, v5, vcc
	v_sub_u32_e32 v6, v0, v3
	v_cmp_gt_i32_e32 vcc, 0, v1
	v_mov_b32_e32 v5, 3
	v_add_u32_e32 v3, v103, v3
	v_cmp_lt_i32_e64 s[2:3], v0, v3
	s_nop 0
	s_and_b64 vcc, vcc, s[2:3]
	v_cndmask_b32_e32 v2, v2, v6, vcc
	v_cndmask_b32_e32 v1, v1, v5, vcc
	v_sub_u32_e32 v6, v0, v3
	v_cmp_gt_i32_e32 vcc, 0, v1
	v_mov_b32_e32 v5, 4
	v_add_u32_e32 v3, v104, v3
	v_cmp_lt_i32_e64 s[2:3], v0, v3
	s_nop 0
	s_and_b64 vcc, vcc, s[2:3]
	v_cndmask_b32_e32 v2, v2, v6, vcc
	v_cndmask_b32_e32 v1, v1, v5, vcc
	v_sub_u32_e32 v6, v0, v3
	v_cmp_gt_i32_e32 vcc, 0, v1
	v_mov_b32_e32 v5, 5
	v_add_u32_e32 v3, v105, v3
	v_cmp_lt_i32_e64 s[2:3], v0, v3
	s_nop 0
	s_and_b64 vcc, vcc, s[2:3]
	v_cndmask_b32_e32 v2, v2, v6, vcc
	v_cndmask_b32_e32 v1, v1, v5, vcc
	v_sub_u32_e32 v6, v0, v3
	v_cmp_gt_i32_e32 vcc, 0, v1
	v_mov_b32_e32 v5, 6
	v_add_u32_e32 v3, v106, v3
	v_cmp_lt_i32_e64 s[2:3], v0, v3
	s_nop 0
	s_and_b64 vcc, vcc, s[2:3]
	v_cndmask_b32_e32 v2, v2, v6, vcc
	v_cndmask_b32_e32 v1, v1, v5, vcc
	v_sub_u32_e32 v6, v0, v3
	v_cmp_gt_i32_e32 vcc, 0, v1
	v_mov_b32_e32 v5, 7
	v_add_u32_e32 v3, v107, v3
	v_cmp_lt_i32_e64 s[2:3], v0, v3
	s_nop 0
	s_and_b64 vcc, vcc, s[2:3]
	v_cndmask_b32_e32 v2, v2, v6, vcc
	v_cndmask_b32_e32 v1, v1, v5, vcc
	v_sub_u32_e32 v6, v0, v3
	v_cmp_gt_i32_e32 vcc, 0, v1
	v_mov_b32_e32 v5, 8
	v_add_u32_e32 v3, v108, v3
	v_cmp_lt_i32_e64 s[2:3], v0, v3
	s_nop 0
	s_and_b64 vcc, vcc, s[2:3]
	v_cndmask_b32_e32 v2, v2, v6, vcc
	v_cndmask_b32_e32 v1, v1, v5, vcc
	v_sub_u32_e32 v6, v0, v3
	v_cmp_gt_i32_e32 vcc, 0, v1
	v_mov_b32_e32 v5, 9
	v_add_u32_e32 v3, v109, v3
	v_cmp_lt_i32_e64 s[2:3], v0, v3
	s_nop 0
	s_and_b64 vcc, vcc, s[2:3]
	v_cndmask_b32_e32 v2, v2, v6, vcc
	v_cndmask_b32_e32 v1, v1, v5, vcc
	v_sub_u32_e32 v6, v0, v3
	v_cmp_gt_i32_e32 vcc, 0, v1
	v_mov_b32_e32 v5, 10
	v_add_u32_e32 v3, v110, v3
	v_cmp_lt_i32_e64 s[2:3], v0, v3
	s_nop 0
	s_and_b64 vcc, vcc, s[2:3]
	v_cndmask_b32_e32 v2, v2, v6, vcc
	v_cndmask_b32_e32 v1, v1, v5, vcc
	v_sub_u32_e32 v6, v0, v3
	v_cmp_gt_i32_e32 vcc, 0, v1
	v_mov_b32_e32 v5, 11
	v_add_u32_e32 v3, v111, v3
	v_cmp_lt_i32_e64 s[2:3], v0, v3
	s_nop 0
	s_and_b64 vcc, vcc, s[2:3]
	v_cndmask_b32_e32 v2, v2, v6, vcc
	v_cndmask_b32_e32 v1, v1, v5, vcc
	v_sub_u32_e32 v6, v0, v3
	v_cmp_gt_i32_e32 vcc, 0, v1
	v_mov_b32_e32 v5, 12
	v_add_u32_e32 v3, v112, v3
	v_cmp_lt_i32_e64 s[2:3], v0, v3
	s_nop 0
	s_and_b64 vcc, vcc, s[2:3]
	v_cndmask_b32_e32 v2, v2, v6, vcc
	v_cndmask_b32_e32 v1, v1, v5, vcc
	v_sub_u32_e32 v6, v0, v3
	v_cmp_gt_i32_e32 vcc, 0, v1
	v_mov_b32_e32 v5, 13
	v_add_u32_e32 v3, v113, v3
	v_cmp_lt_i32_e64 s[2:3], v0, v3
	s_nop 0
	s_and_b64 vcc, vcc, s[2:3]
	v_cndmask_b32_e32 v2, v2, v6, vcc
	v_cndmask_b32_e32 v1, v1, v5, vcc
	v_sub_u32_e32 v6, v0, v3
	v_cmp_gt_i32_e32 vcc, 0, v1
	v_mov_b32_e32 v5, 14
	v_add_u32_e32 v3, v114, v3
	v_cmp_lt_i32_e64 s[2:3], v0, v3
	s_nop 0
	s_and_b64 vcc, vcc, s[2:3]
	v_cndmask_b32_e32 v2, v2, v6, vcc
	v_cndmask_b32_e32 v1, v1, v5, vcc
	v_sub_u32_e32 v6, v0, v3
	v_cmp_gt_i32_e32 vcc, 0, v1
	v_mov_b32_e32 v5, 15
	v_add_u32_e32 v3, v115, v3
	v_cmp_lt_i32_e64 s[2:3], v0, v3
	s_nop 0
	s_and_b64 vcc, vcc, s[2:3]
	v_cndmask_b32_e32 v2, v2, v6, vcc
	v_cndmask_b32_e32 v1, v1, v5, vcc
	v_sub_u32_e32 v6, v0, v3
	v_cmp_gt_i32_e32 vcc, 0, v1
	v_mov_b32_e32 v5, 16
	v_add_u32_e32 v3, v116, v3
	v_cmp_lt_i32_e64 s[2:3], v0, v3
	s_nop 0
	s_and_b64 vcc, vcc, s[2:3]
	v_cndmask_b32_e32 v2, v2, v6, vcc
	v_cndmask_b32_e32 v1, v1, v5, vcc
	v_sub_u32_e32 v6, v0, v3
	v_cmp_gt_i32_e32 vcc, 0, v1
	v_mov_b32_e32 v5, 17
	v_add_u32_e32 v3, v117, v3
	v_cmp_lt_i32_e64 s[2:3], v0, v3
	s_nop 0
	s_and_b64 vcc, vcc, s[2:3]
	v_cndmask_b32_e32 v2, v2, v6, vcc
	v_cndmask_b32_e32 v1, v1, v5, vcc
	v_sub_u32_e32 v6, v0, v3
	v_cmp_gt_i32_e32 vcc, 0, v1
	v_mov_b32_e32 v5, 18
	v_add_u32_e32 v3, v118, v3
	v_cmp_lt_i32_e64 s[2:3], v0, v3
	s_nop 0
	s_and_b64 vcc, vcc, s[2:3]
	v_cndmask_b32_e32 v2, v2, v6, vcc
	v_cndmask_b32_e32 v1, v1, v5, vcc
	v_sub_u32_e32 v6, v0, v3
	v_cmp_gt_i32_e32 vcc, 0, v1
	v_mov_b32_e32 v5, 19
	v_add_u32_e32 v3, v119, v3
	v_cmp_lt_i32_e64 s[2:3], v0, v3
	s_nop 0
	s_and_b64 vcc, vcc, s[2:3]
	v_cndmask_b32_e32 v2, v2, v6, vcc
	v_cndmask_b32_e32 v1, v1, v5, vcc
	v_sub_u32_e32 v6, v0, v3
	v_cmp_gt_i32_e32 vcc, 0, v1
	v_mov_b32_e32 v5, 20
	v_add_u32_e32 v3, v120, v3
	v_cmp_lt_i32_e64 s[2:3], v0, v3
	s_nop 0
	s_and_b64 vcc, vcc, s[2:3]
	v_cndmask_b32_e32 v2, v2, v6, vcc
	v_cndmask_b32_e32 v1, v1, v5, vcc
	v_sub_u32_e32 v6, v0, v3
	v_cmp_gt_i32_e32 vcc, 0, v1
	v_mov_b32_e32 v5, 21
	v_add_u32_e32 v3, v121, v3
	v_cmp_lt_i32_e64 s[2:3], v0, v3
	s_nop 0
	s_and_b64 vcc, vcc, s[2:3]
	v_cndmask_b32_e32 v2, v2, v6, vcc
	v_cndmask_b32_e32 v1, v1, v5, vcc
	v_sub_u32_e32 v6, v0, v3
	v_cmp_gt_i32_e32 vcc, 0, v1
	v_mov_b32_e32 v5, 22
	v_add_u32_e32 v3, v122, v3
	v_cmp_lt_i32_e64 s[2:3], v0, v3
	s_nop 0
	s_and_b64 vcc, vcc, s[2:3]
	v_cndmask_b32_e32 v2, v2, v6, vcc
	v_cndmask_b32_e32 v1, v1, v5, vcc
	v_sub_u32_e32 v6, v0, v3
	v_cmp_gt_i32_e32 vcc, 0, v1
	v_mov_b32_e32 v5, 23
	v_add_u32_e32 v3, v123, v3
	v_cmp_lt_i32_e64 s[2:3], v0, v3
	s_nop 0
	s_and_b64 vcc, vcc, s[2:3]
	v_cndmask_b32_e32 v2, v2, v6, vcc
	v_cndmask_b32_e32 v1, v1, v5, vcc
	v_lshl_or_b32 v2, v1, 16, v2
	v_cmp_lt_i32_e32 vcc, -1, v1
	s_add_i32 s2, 0, 0x22400
	s_nop 0
	v_cndmask_b32_e32 v1, -1, v2, vcc
	v_lshl_add_u32 v2, v0, 2, s2
	ds_write_b32 v2, v1 offset:256
	s_and_b64 exec, exec, s[78:79]
	s_add_i32 s2, 0, 0x224f0
	v_mov_b32_e32 v1, s2
	ds_write_b32 v1, v3
